# MoE down: bias vectors prefetched before the K-loop; out-projection epilogue: both residual load pairs of a row group issued together, one wait per group
# baseline (speedup 1.0000x reference)
.LBB0_1550:
	v_lshl_add_u32 v2, s4, 8, v1
	s_lshl_b32 s34, s30, 8
	v_ashrrev_i32_e32 v3, 31, v2
	s_ashr_i32 s35, s34, 31
	v_lshlrev_b64 v[4:5], 11, v[2:3]
	v_lshl_add_u64 v[12:13], v[4:5], 0, s[34:35]
	v_readlane_b32 s60, v236, 35
	v_or_b32_e32 v14, v12, v170
	v_mov_b32_e32 v15, v13
	v_readlane_b32 s61, v236, 36
	s_nop 15
	s_nop 15
	s_nop 15
	s_andn2_b64 vcc, exec, s[18:19]
	v_readlane_b32 s62, v236, 37
	v_lshl_add_u64 v[8:9], v[14:15], 2, s[60:61]
	global_load_dwordx4 v[4:7], v[8:9], off
	global_load_dwordx4 v[16:19], v[8:9], off offset:16
	v_lshl_add_u64 v[198:199], v[12:13], 0, v[170:171]
	v_lshl_add_u64 v[198:199], v[198:199], 2, s[60:61]
	global_load_dwordx4 v[190:193], v[198:199], off offset:512
	global_load_dwordx4 v[194:197], v[198:199], off offset:528
	v_cndmask_b32_e64 v8, 0, 1, s[18:19]
	v_cmp_ne_u32_e64 s[4:5], 1, v8
	v_readlane_b32 s63, v236, 38
	v_readlane_b32 s64, v236, 39
	v_readlane_b32 s65, v236, 40
	v_readlane_b32 s66, v236, 41
	v_readlane_b32 s67, v236, 42
	v_readlane_b32 s68, v236, 43
	v_readlane_b32 s69, v236, 44
	v_readlane_b32 s70, v236, 45
	v_readlane_b32 s71, v236, 46
	v_readlane_b32 s72, v236, 47
	v_readlane_b32 s73, v236, 48
	v_readlane_b32 s74, v236, 49
	v_readlane_b32 s75, v236, 50
	s_waitcnt vmcnt(0)
	v_pk_fma_f32 v[8:9], v[156:157], s[20:21], v[6:7] op_sel_hi:[1,0,1]
	v_pk_fma_f32 v[10:11], v[154:155], s[20:21], v[4:5] op_sel_hi:[1,0,1]
	v_pk_fma_f32 v[4:5], v[160:161], s[20:21], v[18:19] op_sel_hi:[1,0,1]
	v_pk_fma_f32 v[6:7], v[158:159], s[20:21], v[16:17] op_sel_hi:[1,0,1]
	s_cbranch_vccnz .LBB0_1552
	v_readlane_b32 s60, v236, 24
	v_readlane_b32 s61, v236, 25
	v_cvt_pk_bf16_f32 v16, v10, v11
	v_cvt_pk_bf16_f32 v17, v8, v9
	v_cvt_pk_bf16_f32 v18, v6, v7
	v_cvt_pk_bf16_f32 v19, v4, v5
	v_readlane_b32 s62, v236, 26
	s_nop 0
	v_lshl_add_u64 v[14:15], v[14:15], 1, s[60:61]
	v_readlane_b32 s63, v236, 27
	v_readlane_b32 s64, v236, 28
	v_readlane_b32 s65, v236, 29
	v_readlane_b32 s66, v236, 30
	v_readlane_b32 s67, v236, 31
	global_store_dwordx4 v[14:15], v[16:19], off
.LBB0_1552:
	v_readlane_b32 s60, v236, 35
	v_lshl_add_u64 v[12:13], v[12:13], 0, v[170:171]
	v_readlane_b32 s61, v236, 36
	s_and_b64 vcc, exec, s[4:5]
	v_readlane_b32 s62, v236, 37
	v_readlane_b32 s63, v236, 38
	v_readlane_b32 s64, v236, 39
	v_readlane_b32 s65, v236, 40
	v_readlane_b32 s66, v236, 41
	v_readlane_b32 s67, v236, 42
	v_readlane_b32 s68, v236, 43
	v_readlane_b32 s69, v236, 44
	v_readlane_b32 s70, v236, 45
	v_readlane_b32 s71, v236, 46
	v_readlane_b32 s72, v236, 47
	v_readlane_b32 s73, v236, 48
	v_readlane_b32 s74, v236, 49
	v_readlane_b32 s75, v236, 50
	v_pk_fma_f32 v[18:19], v[148:149], s[20:21], v[192:193] op_sel_hi:[1,0,1]
	v_pk_fma_f32 v[20:21], v[146:147], s[20:21], v[190:191] op_sel_hi:[1,0,1]
	v_pk_fma_f32 v[14:15], v[152:153], s[20:21], v[196:197] op_sel_hi:[1,0,1]
	v_pk_fma_f32 v[16:17], v[150:151], s[20:21], v[194:195] op_sel_hi:[1,0,1]
	s_cbranch_vccnz .LBB0_1554
	v_readlane_b32 s60, v236, 24
	v_readlane_b32 s61, v236, 25
	v_cvt_pk_bf16_f32 v22, v20, v21
	v_cvt_pk_bf16_f32 v23, v18, v19
	v_cvt_pk_bf16_f32 v24, v16, v17
	v_cvt_pk_bf16_f32 v25, v14, v15
	v_readlane_b32 s62, v236, 26
	s_nop 0
	v_lshl_add_u64 v[12:13], v[12:13], 1, s[60:61]
	v_readlane_b32 s63, v236, 27
	v_readlane_b32 s64, v236, 28
	v_readlane_b32 s65, v236, 29
	v_readlane_b32 s66, v236, 30
	v_readlane_b32 s67, v236, 31
	global_store_dwordx4 v[12:13], v[22:25], off offset:256

.LBB0_1556:
	s_or_b64 exec, exec, s[30:31]
	v_or_b32_e32 v4, 16, v2
	v_ashrrev_i32_e32 v5, 31, v4
	v_lshlrev_b64 v[6:7], 11, v[4:5]
	v_lshl_add_u64 v[14:15], v[6:7], 0, s[34:35]
	v_readlane_b32 s60, v236, 35
	v_or_b32_e32 v16, v14, v170
	v_mov_b32_e32 v17, v15
	v_readlane_b32 s61, v236, 36
	s_and_b64 vcc, exec, s[4:5]
	v_readlane_b32 s62, v236, 37
	v_lshl_add_u64 v[10:11], v[16:17], 2, s[60:61]
	global_load_dwordx4 v[6:9], v[10:11], off
	global_load_dwordx4 v[18:21], v[10:11], off offset:16
	v_lshl_add_u64 v[198:199], v[14:15], 0, v[170:171]
	v_lshl_add_u64 v[198:199], v[198:199], 2, s[60:61]
	global_load_dwordx4 v[190:193], v[198:199], off offset:512
	global_load_dwordx4 v[194:197], v[198:199], off offset:528
	v_readlane_b32 s63, v236, 38
	v_readlane_b32 s64, v236, 39
	v_readlane_b32 s65, v236, 40
	v_readlane_b32 s66, v236, 41
	v_readlane_b32 s67, v236, 42
	v_readlane_b32 s68, v236, 43
	v_readlane_b32 s69, v236, 44
	v_readlane_b32 s70, v236, 45
	v_readlane_b32 s71, v236, 46
	v_readlane_b32 s72, v236, 47
	v_readlane_b32 s73, v236, 48
	v_readlane_b32 s74, v236, 49
	v_readlane_b32 s75, v236, 50
	s_waitcnt vmcnt(0)
	v_pk_fma_f32 v[10:11], v[140:141], s[20:21], v[8:9] op_sel_hi:[1,0,1]
	v_pk_fma_f32 v[12:13], v[138:139], s[20:21], v[6:7] op_sel_hi:[1,0,1]
	v_pk_fma_f32 v[6:7], v[144:145], s[20:21], v[20:21] op_sel_hi:[1,0,1]
	v_pk_fma_f32 v[8:9], v[142:143], s[20:21], v[18:19] op_sel_hi:[1,0,1]
	s_cbranch_vccnz .LBB0_1558
	v_readlane_b32 s60, v236, 24
	v_readlane_b32 s61, v236, 25
	v_cvt_pk_bf16_f32 v18, v12, v13
	v_cvt_pk_bf16_f32 v19, v10, v11
	v_cvt_pk_bf16_f32 v20, v8, v9
	v_cvt_pk_bf16_f32 v21, v6, v7
	v_readlane_b32 s62, v236, 26
	s_nop 0
	v_lshl_add_u64 v[16:17], v[16:17], 1, s[60:61]
	v_readlane_b32 s63, v236, 27
	v_readlane_b32 s64, v236, 28
	v_readlane_b32 s65, v236, 29
	v_readlane_b32 s66, v236, 30
	v_readlane_b32 s67, v236, 31
	global_store_dwordx4 v[16:17], v[18:21], off
.LBB0_1558:
	v_readlane_b32 s60, v236, 35
	v_lshl_add_u64 v[14:15], v[14:15], 0, v[170:171]
	v_readlane_b32 s61, v236, 36
	s_and_b64 vcc, exec, s[4:5]
	v_readlane_b32 s62, v236, 37
	v_readlane_b32 s63, v236, 38
	v_readlane_b32 s64, v236, 39
	v_readlane_b32 s65, v236, 40
	v_readlane_b32 s66, v236, 41
	v_readlane_b32 s67, v236, 42
	v_readlane_b32 s68, v236, 43
	v_readlane_b32 s69, v236, 44
	v_readlane_b32 s70, v236, 45
	v_readlane_b32 s71, v236, 46
	v_readlane_b32 s72, v236, 47
	v_readlane_b32 s73, v236, 48
	v_readlane_b32 s74, v236, 49
	v_readlane_b32 s75, v236, 50
	v_pk_fma_f32 v[20:21], v[132:133], s[20:21], v[192:193] op_sel_hi:[1,0,1]
	v_pk_fma_f32 v[22:23], v[130:131], s[20:21], v[190:191] op_sel_hi:[1,0,1]
	v_pk_fma_f32 v[16:17], v[136:137], s[20:21], v[196:197] op_sel_hi:[1,0,1]
	v_pk_fma_f32 v[18:19], v[134:135], s[20:21], v[194:195] op_sel_hi:[1,0,1]
	s_cbranch_vccnz .LBB0_1560
	v_readlane_b32 s60, v236, 24
	v_readlane_b32 s61, v236, 25
	v_cvt_pk_bf16_f32 v24, v22, v23
	v_cvt_pk_bf16_f32 v25, v20, v21
	v_cvt_pk_bf16_f32 v26, v18, v19
	v_cvt_pk_bf16_f32 v27, v16, v17
	v_readlane_b32 s62, v236, 26
	s_nop 0
	v_lshl_add_u64 v[14:15], v[14:15], 1, s[60:61]
	v_readlane_b32 s63, v236, 27
	v_readlane_b32 s64, v236, 28
	v_readlane_b32 s65, v236, 29
	v_readlane_b32 s66, v236, 30
	v_readlane_b32 s67, v236, 31
	global_store_dwordx4 v[14:15], v[24:27], off offset:256

.LBB0_1562:
	s_or_b64 exec, exec, s[30:31]
	v_or_b32_e32 v4, 32, v2
	v_ashrrev_i32_e32 v5, 31, v4
	v_lshlrev_b64 v[6:7], 11, v[4:5]
	v_lshl_add_u64 v[14:15], v[6:7], 0, s[34:35]
	v_readlane_b32 s60, v236, 35
	v_or_b32_e32 v16, v14, v170
	v_mov_b32_e32 v17, v15
	v_readlane_b32 s61, v236, 36
	s_and_b64 vcc, exec, s[4:5]
	v_readlane_b32 s62, v236, 37
	v_lshl_add_u64 v[10:11], v[16:17], 2, s[60:61]
	global_load_dwordx4 v[6:9], v[10:11], off
	global_load_dwordx4 v[18:21], v[10:11], off offset:16
	v_lshl_add_u64 v[198:199], v[14:15], 0, v[170:171]
	v_lshl_add_u64 v[198:199], v[198:199], 2, s[60:61]
	global_load_dwordx4 v[190:193], v[198:199], off offset:512
	global_load_dwordx4 v[194:197], v[198:199], off offset:528
	v_readlane_b32 s63, v236, 38
	v_readlane_b32 s64, v236, 39
	v_readlane_b32 s65, v236, 40
	v_readlane_b32 s66, v236, 41
	v_readlane_b32 s67, v236, 42
	v_readlane_b32 s68, v236, 43
	v_readlane_b32 s69, v236, 44
	v_readlane_b32 s70, v236, 45
	v_readlane_b32 s71, v236, 46
	v_readlane_b32 s72, v236, 47
	v_readlane_b32 s73, v236, 48
	v_readlane_b32 s74, v236, 49
	v_readlane_b32 s75, v236, 50
	s_waitcnt vmcnt(0)
	v_pk_fma_f32 v[10:11], v[124:125], s[20:21], v[8:9] op_sel_hi:[1,0,1]
	v_pk_fma_f32 v[12:13], v[122:123], s[20:21], v[6:7] op_sel_hi:[1,0,1]
	v_pk_fma_f32 v[6:7], v[128:129], s[20:21], v[20:21] op_sel_hi:[1,0,1]
	v_pk_fma_f32 v[8:9], v[126:127], s[20:21], v[18:19] op_sel_hi:[1,0,1]
	s_cbranch_vccnz .LBB0_1564
	v_readlane_b32 s60, v236, 24
	v_readlane_b32 s61, v236, 25
	v_cvt_pk_bf16_f32 v18, v12, v13
	v_cvt_pk_bf16_f32 v19, v10, v11
	v_cvt_pk_bf16_f32 v20, v8, v9
	v_cvt_pk_bf16_f32 v21, v6, v7
	v_readlane_b32 s62, v236, 26
	s_nop 0
	v_lshl_add_u64 v[16:17], v[16:17], 1, s[60:61]
	v_readlane_b32 s63, v236, 27
	v_readlane_b32 s64, v236, 28
	v_readlane_b32 s65, v236, 29
	v_readlane_b32 s66, v236, 30
	v_readlane_b32 s67, v236, 31
	global_store_dwordx4 v[16:17], v[18:21], off
.LBB0_1564:
	v_readlane_b32 s60, v236, 35
	v_lshl_add_u64 v[14:15], v[14:15], 0, v[170:171]
	v_readlane_b32 s61, v236, 36
	s_and_b64 vcc, exec, s[4:5]
	v_readlane_b32 s62, v236, 37
	v_readlane_b32 s63, v236, 38
	v_readlane_b32 s64, v236, 39
	v_readlane_b32 s65, v236, 40
	v_readlane_b32 s66, v236, 41
	v_readlane_b32 s67, v236, 42
	v_readlane_b32 s68, v236, 43
	v_readlane_b32 s69, v236, 44
	v_readlane_b32 s70, v236, 45
	v_readlane_b32 s71, v236, 46
	v_readlane_b32 s72, v236, 47
	v_readlane_b32 s73, v236, 48
	v_readlane_b32 s74, v236, 49
	v_readlane_b32 s75, v236, 50
	v_pk_fma_f32 v[20:21], v[116:117], s[20:21], v[192:193] op_sel_hi:[1,0,1]
	v_pk_fma_f32 v[22:23], v[114:115], s[20:21], v[190:191] op_sel_hi:[1,0,1]
	v_pk_fma_f32 v[16:17], v[120:121], s[20:21], v[196:197] op_sel_hi:[1,0,1]
	v_pk_fma_f32 v[18:19], v[118:119], s[20:21], v[194:195] op_sel_hi:[1,0,1]
	s_cbranch_vccnz .LBB0_1566
	v_readlane_b32 s60, v236, 24
	v_readlane_b32 s61, v236, 25
	v_cvt_pk_bf16_f32 v24, v22, v23
	v_cvt_pk_bf16_f32 v25, v20, v21
	v_cvt_pk_bf16_f32 v26, v18, v19
	v_cvt_pk_bf16_f32 v27, v16, v17
	v_readlane_b32 s62, v236, 26
	s_nop 0
	v_lshl_add_u64 v[14:15], v[14:15], 1, s[60:61]
	v_readlane_b32 s63, v236, 27
	v_readlane_b32 s64, v236, 28
	v_readlane_b32 s65, v236, 29
	v_readlane_b32 s66, v236, 30
	v_readlane_b32 s67, v236, 31
	global_store_dwordx4 v[14:15], v[24:27], off offset:256

.LBB0_1568:
	s_or_b64 exec, exec, s[30:31]
	v_or_b32_e32 v4, 48, v2
	v_ashrrev_i32_e32 v5, 31, v4
	v_lshlrev_b64 v[6:7], 11, v[4:5]
	v_lshl_add_u64 v[14:15], v[6:7], 0, s[34:35]
	v_readlane_b32 s60, v236, 35
	v_or_b32_e32 v16, v14, v170
	v_mov_b32_e32 v17, v15
	v_readlane_b32 s61, v236, 36
	s_and_b64 vcc, exec, s[4:5]
	v_readlane_b32 s62, v236, 37
	v_lshl_add_u64 v[10:11], v[16:17], 2, s[60:61]
	global_load_dwordx4 v[6:9], v[10:11], off
	global_load_dwordx4 v[18:21], v[10:11], off offset:16
	v_lshl_add_u64 v[198:199], v[14:15], 0, v[170:171]
	v_lshl_add_u64 v[198:199], v[198:199], 2, s[60:61]
	global_load_dwordx4 v[190:193], v[198:199], off offset:512
	global_load_dwordx4 v[194:197], v[198:199], off offset:528
	v_readlane_b32 s63, v236, 38
	v_readlane_b32 s64, v236, 39
	v_readlane_b32 s65, v236, 40
	v_readlane_b32 s66, v236, 41
	v_readlane_b32 s67, v236, 42
	v_readlane_b32 s68, v236, 43
	v_readlane_b32 s69, v236, 44
	v_readlane_b32 s70, v236, 45
	v_readlane_b32 s71, v236, 46
	v_readlane_b32 s72, v236, 47
	v_readlane_b32 s73, v236, 48
	v_readlane_b32 s74, v236, 49
	v_readlane_b32 s75, v236, 50
	s_waitcnt vmcnt(0)
	v_pk_fma_f32 v[10:11], v[108:109], s[20:21], v[8:9] op_sel_hi:[1,0,1]
	v_pk_fma_f32 v[12:13], v[106:107], s[20:21], v[6:7] op_sel_hi:[1,0,1]
	v_pk_fma_f32 v[6:7], v[112:113], s[20:21], v[20:21] op_sel_hi:[1,0,1]
	v_pk_fma_f32 v[8:9], v[110:111], s[20:21], v[18:19] op_sel_hi:[1,0,1]
	s_cbranch_vccnz .LBB0_1570
	v_readlane_b32 s60, v236, 24
	v_readlane_b32 s61, v236, 25
	v_cvt_pk_bf16_f32 v18, v12, v13
	v_cvt_pk_bf16_f32 v19, v10, v11
	v_cvt_pk_bf16_f32 v20, v8, v9
	v_cvt_pk_bf16_f32 v21, v6, v7
	v_readlane_b32 s62, v236, 26
	s_nop 0
	v_lshl_add_u64 v[16:17], v[16:17], 1, s[60:61]
	v_readlane_b32 s63, v236, 27
	v_readlane_b32 s64, v236, 28
	v_readlane_b32 s65, v236, 29
	v_readlane_b32 s66, v236, 30
	v_readlane_b32 s67, v236, 31
	global_store_dwordx4 v[16:17], v[18:21], off
.LBB0_1570:
	v_readlane_b32 s60, v236, 35
	v_lshl_add_u64 v[14:15], v[14:15], 0, v[170:171]
	v_readlane_b32 s61, v236, 36
	s_and_b64 vcc, exec, s[4:5]
	v_readlane_b32 s62, v236, 37
	v_readlane_b32 s63, v236, 38
	v_readlane_b32 s64, v236, 39
	v_readlane_b32 s65, v236, 40
	v_readlane_b32 s66, v236, 41
	v_readlane_b32 s67, v236, 42
	v_readlane_b32 s68, v236, 43
	v_readlane_b32 s69, v236, 44
	v_readlane_b32 s70, v236, 45
	v_readlane_b32 s71, v236, 46
	v_readlane_b32 s72, v236, 47
	v_readlane_b32 s73, v236, 48
	v_readlane_b32 s74, v236, 49
	v_readlane_b32 s75, v236, 50
	v_pk_fma_f32 v[20:21], v[100:101], s[20:21], v[192:193] op_sel_hi:[1,0,1]
	v_pk_fma_f32 v[22:23], v[98:99], s[20:21], v[190:191] op_sel_hi:[1,0,1]
	v_pk_fma_f32 v[16:17], v[104:105], s[20:21], v[196:197] op_sel_hi:[1,0,1]
	v_pk_fma_f32 v[18:19], v[102:103], s[20:21], v[194:195] op_sel_hi:[1,0,1]
	s_cbranch_vccnz .LBB0_1572
	v_readlane_b32 s60, v236, 24
	v_readlane_b32 s61, v236, 25
	v_cvt_pk_bf16_f32 v24, v22, v23
	v_cvt_pk_bf16_f32 v25, v20, v21
	v_cvt_pk_bf16_f32 v26, v18, v19
	v_cvt_pk_bf16_f32 v27, v16, v17
	v_readlane_b32 s62, v236, 26
	s_nop 0
	v_lshl_add_u64 v[14:15], v[14:15], 1, s[60:61]
	v_readlane_b32 s63, v236, 27
	v_readlane_b32 s64, v236, 28
	v_readlane_b32 s65, v236, 29
	v_readlane_b32 s66, v236, 30
	v_readlane_b32 s67, v236, 31
	global_store_dwordx4 v[14:15], v[24:27], off offset:256

.LBB0_1574:
	s_or_b64 exec, exec, s[30:31]
	v_add_u32_e32 v4, 0x80, v2
	v_ashrrev_i32_e32 v5, 31, v4
	v_lshlrev_b64 v[6:7], 11, v[4:5]
	v_lshl_add_u64 v[14:15], v[6:7], 0, s[34:35]
	v_readlane_b32 s60, v236, 35
	v_or_b32_e32 v16, v14, v170
	v_mov_b32_e32 v17, v15
	v_readlane_b32 s61, v236, 36
	s_and_b64 vcc, exec, s[4:5]
	v_readlane_b32 s62, v236, 37
	v_lshl_add_u64 v[10:11], v[16:17], 2, s[60:61]
	global_load_dwordx4 v[6:9], v[10:11], off
	global_load_dwordx4 v[18:21], v[10:11], off offset:16
	v_lshl_add_u64 v[198:199], v[14:15], 0, v[170:171]
	v_lshl_add_u64 v[198:199], v[198:199], 2, s[60:61]
	global_load_dwordx4 v[190:193], v[198:199], off offset:512
	global_load_dwordx4 v[194:197], v[198:199], off offset:528
	v_readlane_b32 s63, v236, 38
	v_readlane_b32 s64, v236, 39
	v_readlane_b32 s65, v236, 40
	v_readlane_b32 s66, v236, 41
	v_readlane_b32 s67, v236, 42
	v_readlane_b32 s68, v236, 43
	v_readlane_b32 s69, v236, 44
	v_readlane_b32 s70, v236, 45
	v_readlane_b32 s71, v236, 46
	v_readlane_b32 s72, v236, 47
	v_readlane_b32 s73, v236, 48
	v_readlane_b32 s74, v236, 49
	v_readlane_b32 s75, v236, 50
	s_waitcnt vmcnt(0)
	v_pk_fma_f32 v[10:11], v[92:93], s[20:21], v[8:9] op_sel_hi:[1,0,1]
	v_pk_fma_f32 v[12:13], v[90:91], s[20:21], v[6:7] op_sel_hi:[1,0,1]
	v_pk_fma_f32 v[6:7], v[96:97], s[20:21], v[20:21] op_sel_hi:[1,0,1]
	v_pk_fma_f32 v[8:9], v[94:95], s[20:21], v[18:19] op_sel_hi:[1,0,1]
	s_cbranch_vccnz .LBB0_1576
	v_readlane_b32 s60, v236, 24
	v_readlane_b32 s61, v236, 25
	v_cvt_pk_bf16_f32 v18, v12, v13
	v_cvt_pk_bf16_f32 v19, v10, v11
	v_cvt_pk_bf16_f32 v20, v8, v9
	v_cvt_pk_bf16_f32 v21, v6, v7
	v_readlane_b32 s62, v236, 26
	s_nop 0
	v_lshl_add_u64 v[16:17], v[16:17], 1, s[60:61]
	v_readlane_b32 s63, v236, 27
	v_readlane_b32 s64, v236, 28
	v_readlane_b32 s65, v236, 29
	v_readlane_b32 s66, v236, 30
	v_readlane_b32 s67, v236, 31
	global_store_dwordx4 v[16:17], v[18:21], off
.LBB0_1576:
	v_readlane_b32 s60, v236, 35
	v_lshl_add_u64 v[14:15], v[14:15], 0, v[170:171]
	v_readlane_b32 s61, v236, 36
	s_and_b64 vcc, exec, s[4:5]
	v_readlane_b32 s62, v236, 37
	v_readlane_b32 s63, v236, 38
	v_readlane_b32 s64, v236, 39
	v_readlane_b32 s65, v236, 40
	v_readlane_b32 s66, v236, 41
	v_readlane_b32 s67, v236, 42
	v_readlane_b32 s68, v236, 43
	v_readlane_b32 s69, v236, 44
	v_readlane_b32 s70, v236, 45
	v_readlane_b32 s71, v236, 46
	v_readlane_b32 s72, v236, 47
	v_readlane_b32 s73, v236, 48
	v_readlane_b32 s74, v236, 49
	v_readlane_b32 s75, v236, 50
	v_pk_fma_f32 v[20:21], v[84:85], s[20:21], v[192:193] op_sel_hi:[1,0,1]
	v_pk_fma_f32 v[22:23], v[82:83], s[20:21], v[190:191] op_sel_hi:[1,0,1]
	v_pk_fma_f32 v[16:17], v[88:89], s[20:21], v[196:197] op_sel_hi:[1,0,1]
	v_pk_fma_f32 v[18:19], v[86:87], s[20:21], v[194:195] op_sel_hi:[1,0,1]
	s_cbranch_vccnz .LBB0_1578
	v_readlane_b32 s60, v236, 24
	v_readlane_b32 s61, v236, 25
	v_cvt_pk_bf16_f32 v24, v22, v23
	v_cvt_pk_bf16_f32 v25, v20, v21
	v_cvt_pk_bf16_f32 v26, v18, v19
	v_cvt_pk_bf16_f32 v27, v16, v17
	v_readlane_b32 s62, v236, 26
	s_nop 0
	v_lshl_add_u64 v[14:15], v[14:15], 1, s[60:61]
	v_readlane_b32 s63, v236, 27
	v_readlane_b32 s64, v236, 28
	v_readlane_b32 s65, v236, 29
	v_readlane_b32 s66, v236, 30
	v_readlane_b32 s67, v236, 31
	global_store_dwordx4 v[14:15], v[24:27], off offset:256

.LBB0_1580:
	s_or_b64 exec, exec, s[30:31]
	v_add_u32_e32 v4, 0x90, v2
	v_ashrrev_i32_e32 v5, 31, v4
	v_lshlrev_b64 v[6:7], 11, v[4:5]
	v_lshl_add_u64 v[14:15], v[6:7], 0, s[34:35]
	v_readlane_b32 s60, v236, 35
	v_or_b32_e32 v16, v14, v170
	v_mov_b32_e32 v17, v15
	v_readlane_b32 s61, v236, 36
	s_and_b64 vcc, exec, s[4:5]
	v_readlane_b32 s62, v236, 37
	v_lshl_add_u64 v[10:11], v[16:17], 2, s[60:61]
	global_load_dwordx4 v[6:9], v[10:11], off
	global_load_dwordx4 v[18:21], v[10:11], off offset:16
	v_lshl_add_u64 v[198:199], v[14:15], 0, v[170:171]
	v_lshl_add_u64 v[198:199], v[198:199], 2, s[60:61]
	global_load_dwordx4 v[190:193], v[198:199], off offset:512
	global_load_dwordx4 v[194:197], v[198:199], off offset:528
	v_readlane_b32 s63, v236, 38
	v_readlane_b32 s64, v236, 39
	v_readlane_b32 s65, v236, 40
	v_readlane_b32 s66, v236, 41
	v_readlane_b32 s67, v236, 42
	v_readlane_b32 s68, v236, 43
	v_readlane_b32 s69, v236, 44
	v_readlane_b32 s70, v236, 45
	v_readlane_b32 s71, v236, 46
	v_readlane_b32 s72, v236, 47
	v_readlane_b32 s73, v236, 48
	v_readlane_b32 s74, v236, 49
	v_readlane_b32 s75, v236, 50
	s_waitcnt vmcnt(0)
	v_pk_fma_f32 v[10:11], v[76:77], s[20:21], v[8:9] op_sel_hi:[1,0,1]
	v_pk_fma_f32 v[12:13], v[74:75], s[20:21], v[6:7] op_sel_hi:[1,0,1]
	v_pk_fma_f32 v[6:7], v[80:81], s[20:21], v[20:21] op_sel_hi:[1,0,1]
	v_pk_fma_f32 v[8:9], v[78:79], s[20:21], v[18:19] op_sel_hi:[1,0,1]
	s_cbranch_vccnz .LBB0_1582
	v_readlane_b32 s60, v236, 24
	v_readlane_b32 s61, v236, 25
	v_cvt_pk_bf16_f32 v18, v12, v13
	v_cvt_pk_bf16_f32 v19, v10, v11
	v_cvt_pk_bf16_f32 v20, v8, v9
	v_cvt_pk_bf16_f32 v21, v6, v7
	v_readlane_b32 s62, v236, 26
	s_nop 0
	v_lshl_add_u64 v[16:17], v[16:17], 1, s[60:61]
	v_readlane_b32 s63, v236, 27
	v_readlane_b32 s64, v236, 28
	v_readlane_b32 s65, v236, 29
	v_readlane_b32 s66, v236, 30
	v_readlane_b32 s67, v236, 31
	global_store_dwordx4 v[16:17], v[18:21], off
.LBB0_1582:
	v_readlane_b32 s60, v236, 35
	v_lshl_add_u64 v[14:15], v[14:15], 0, v[170:171]
	v_readlane_b32 s61, v236, 36
	s_and_b64 vcc, exec, s[4:5]
	v_readlane_b32 s62, v236, 37
	v_readlane_b32 s63, v236, 38
	v_readlane_b32 s64, v236, 39
	v_readlane_b32 s65, v236, 40
	v_readlane_b32 s66, v236, 41
	v_readlane_b32 s67, v236, 42
	v_readlane_b32 s68, v236, 43
	v_readlane_b32 s69, v236, 44
	v_readlane_b32 s70, v236, 45
	v_readlane_b32 s71, v236, 46
	v_readlane_b32 s72, v236, 47
	v_readlane_b32 s73, v236, 48
	v_readlane_b32 s74, v236, 49
	v_readlane_b32 s75, v236, 50
	v_pk_fma_f32 v[20:21], v[68:69], s[20:21], v[192:193] op_sel_hi:[1,0,1]
	v_pk_fma_f32 v[22:23], v[66:67], s[20:21], v[190:191] op_sel_hi:[1,0,1]
	v_pk_fma_f32 v[16:17], v[72:73], s[20:21], v[196:197] op_sel_hi:[1,0,1]
	v_pk_fma_f32 v[18:19], v[70:71], s[20:21], v[194:195] op_sel_hi:[1,0,1]
	s_cbranch_vccnz .LBB0_1584
	v_readlane_b32 s60, v236, 24
	v_readlane_b32 s61, v236, 25
	v_cvt_pk_bf16_f32 v24, v22, v23
	v_cvt_pk_bf16_f32 v25, v20, v21
	v_cvt_pk_bf16_f32 v26, v18, v19
	v_cvt_pk_bf16_f32 v27, v16, v17
	v_readlane_b32 s62, v236, 26
	s_nop 0
	v_lshl_add_u64 v[14:15], v[14:15], 1, s[60:61]
	v_readlane_b32 s63, v236, 27
	v_readlane_b32 s64, v236, 28
	v_readlane_b32 s65, v236, 29
	v_readlane_b32 s66, v236, 30
	v_readlane_b32 s67, v236, 31
	global_store_dwordx4 v[14:15], v[24:27], off offset:256

.LBB0_1586:
	s_or_b64 exec, exec, s[30:31]
	v_add_u32_e32 v4, 0xa0, v2
	v_ashrrev_i32_e32 v5, 31, v4
	v_lshlrev_b64 v[6:7], 11, v[4:5]
	v_lshl_add_u64 v[14:15], v[6:7], 0, s[34:35]
	v_readlane_b32 s60, v236, 35
	v_or_b32_e32 v16, v14, v170
	v_mov_b32_e32 v17, v15
	v_readlane_b32 s61, v236, 36
	s_and_b64 vcc, exec, s[4:5]
	v_readlane_b32 s62, v236, 37
	v_lshl_add_u64 v[10:11], v[16:17], 2, s[60:61]
	global_load_dwordx4 v[6:9], v[10:11], off
	global_load_dwordx4 v[18:21], v[10:11], off offset:16
	v_lshl_add_u64 v[198:199], v[14:15], 0, v[170:171]
	v_lshl_add_u64 v[198:199], v[198:199], 2, s[60:61]
	global_load_dwordx4 v[190:193], v[198:199], off offset:512
	global_load_dwordx4 v[194:197], v[198:199], off offset:528
	v_readlane_b32 s63, v236, 38
	v_readlane_b32 s64, v236, 39
	v_readlane_b32 s65, v236, 40
	v_readlane_b32 s66, v236, 41
	v_readlane_b32 s67, v236, 42
	v_readlane_b32 s68, v236, 43
	v_readlane_b32 s69, v236, 44
	v_readlane_b32 s70, v236, 45
	v_readlane_b32 s71, v236, 46
	v_readlane_b32 s72, v236, 47
	v_readlane_b32 s73, v236, 48
	v_readlane_b32 s74, v236, 49
	v_readlane_b32 s75, v236, 50
	s_waitcnt vmcnt(0)
	v_pk_fma_f32 v[10:11], v[60:61], s[20:21], v[8:9] op_sel_hi:[1,0,1]
	v_pk_fma_f32 v[12:13], v[58:59], s[20:21], v[6:7] op_sel_hi:[1,0,1]
	v_pk_fma_f32 v[6:7], v[64:65], s[20:21], v[20:21] op_sel_hi:[1,0,1]
	v_pk_fma_f32 v[8:9], v[62:63], s[20:21], v[18:19] op_sel_hi:[1,0,1]
	s_cbranch_vccnz .LBB0_1588
	v_readlane_b32 s60, v236, 24
	v_readlane_b32 s61, v236, 25
	v_cvt_pk_bf16_f32 v18, v12, v13
	v_cvt_pk_bf16_f32 v19, v10, v11
	v_cvt_pk_bf16_f32 v20, v8, v9
	v_cvt_pk_bf16_f32 v21, v6, v7
	v_readlane_b32 s62, v236, 26
	s_nop 0
	v_lshl_add_u64 v[16:17], v[16:17], 1, s[60:61]
	v_readlane_b32 s63, v236, 27
	v_readlane_b32 s64, v236, 28
	v_readlane_b32 s65, v236, 29
	v_readlane_b32 s66, v236, 30
	v_readlane_b32 s67, v236, 31
	global_store_dwordx4 v[16:17], v[18:21], off
.LBB0_1588:
	v_readlane_b32 s60, v236, 35
	v_lshl_add_u64 v[14:15], v[14:15], 0, v[170:171]
	v_readlane_b32 s61, v236, 36
	s_and_b64 vcc, exec, s[4:5]
	v_readlane_b32 s62, v236, 37
	v_readlane_b32 s63, v236, 38
	v_readlane_b32 s64, v236, 39
	v_readlane_b32 s65, v236, 40
	v_readlane_b32 s66, v236, 41
	v_readlane_b32 s67, v236, 42
	v_readlane_b32 s68, v236, 43
	v_readlane_b32 s69, v236, 44
	v_readlane_b32 s70, v236, 45
	v_readlane_b32 s71, v236, 46
	v_readlane_b32 s72, v236, 47
	v_readlane_b32 s73, v236, 48
	v_readlane_b32 s74, v236, 49
	v_readlane_b32 s75, v236, 50
	v_pk_fma_f32 v[20:21], v[52:53], s[20:21], v[192:193] op_sel_hi:[1,0,1]
	v_pk_fma_f32 v[22:23], v[50:51], s[20:21], v[190:191] op_sel_hi:[1,0,1]
	v_pk_fma_f32 v[16:17], v[56:57], s[20:21], v[196:197] op_sel_hi:[1,0,1]
	v_pk_fma_f32 v[18:19], v[54:55], s[20:21], v[194:195] op_sel_hi:[1,0,1]
	s_cbranch_vccnz .LBB0_1590
	v_readlane_b32 s60, v236, 24
	v_readlane_b32 s61, v236, 25
	v_cvt_pk_bf16_f32 v24, v22, v23
	v_cvt_pk_bf16_f32 v25, v20, v21
	v_cvt_pk_bf16_f32 v26, v18, v19
	v_cvt_pk_bf16_f32 v27, v16, v17
	v_readlane_b32 s62, v236, 26
	s_nop 0
	v_lshl_add_u64 v[14:15], v[14:15], 1, s[60:61]
	v_readlane_b32 s63, v236, 27
	v_readlane_b32 s64, v236, 28
	v_readlane_b32 s65, v236, 29
	v_readlane_b32 s66, v236, 30
	v_readlane_b32 s67, v236, 31
	global_store_dwordx4 v[14:15], v[24:27], off offset:256

.LBB0_1592:
	s_or_b64 exec, exec, s[30:31]
	v_add_u32_e32 v2, 0xb0, v2
	v_ashrrev_i32_e32 v3, 31, v2
	v_lshlrev_b64 v[4:5], 11, v[2:3]
	v_lshl_add_u64 v[12:13], v[4:5], 0, s[34:35]
	v_readlane_b32 s60, v236, 35
	v_or_b32_e32 v14, v12, v170
	v_mov_b32_e32 v15, v13
	v_readlane_b32 s61, v236, 36
	s_and_b64 vcc, exec, s[4:5]
	v_readlane_b32 s62, v236, 37
	v_lshl_add_u64 v[8:9], v[14:15], 2, s[60:61]
	global_load_dwordx4 v[4:7], v[8:9], off
	global_load_dwordx4 v[16:19], v[8:9], off offset:16
	v_lshl_add_u64 v[198:199], v[12:13], 0, v[170:171]
	v_lshl_add_u64 v[198:199], v[198:199], 2, s[60:61]
	global_load_dwordx4 v[190:193], v[198:199], off offset:512
	global_load_dwordx4 v[194:197], v[198:199], off offset:528
	v_readlane_b32 s63, v236, 38
	v_readlane_b32 s64, v236, 39
	v_readlane_b32 s65, v236, 40
	v_readlane_b32 s66, v236, 41
	v_readlane_b32 s67, v236, 42
	v_readlane_b32 s68, v236, 43
	v_readlane_b32 s69, v236, 44
	v_readlane_b32 s70, v236, 45
	v_readlane_b32 s71, v236, 46
	v_readlane_b32 s72, v236, 47
	v_readlane_b32 s73, v236, 48
	v_readlane_b32 s74, v236, 49
	v_readlane_b32 s75, v236, 50
	s_waitcnt vmcnt(0)
	v_pk_fma_f32 v[8:9], v[44:45], s[20:21], v[6:7] op_sel_hi:[1,0,1]
	v_pk_fma_f32 v[10:11], v[42:43], s[20:21], v[4:5] op_sel_hi:[1,0,1]
	v_pk_fma_f32 v[4:5], v[48:49], s[20:21], v[18:19] op_sel_hi:[1,0,1]
	v_pk_fma_f32 v[6:7], v[46:47], s[20:21], v[16:17] op_sel_hi:[1,0,1]
	s_cbranch_vccnz .LBB0_1594
	v_readlane_b32 s60, v236, 24
	v_readlane_b32 s61, v236, 25
	v_cvt_pk_bf16_f32 v16, v10, v11
	v_cvt_pk_bf16_f32 v17, v8, v9
	v_cvt_pk_bf16_f32 v18, v6, v7
	v_cvt_pk_bf16_f32 v19, v4, v5
	v_readlane_b32 s62, v236, 26
	s_nop 0
	v_lshl_add_u64 v[14:15], v[14:15], 1, s[60:61]
	v_readlane_b32 s63, v236, 27
	v_readlane_b32 s64, v236, 28
	v_readlane_b32 s65, v236, 29
	v_readlane_b32 s66, v236, 30
	v_readlane_b32 s67, v236, 31
	global_store_dwordx4 v[14:15], v[16:19], off
.LBB0_1594:
	v_readlane_b32 s60, v236, 35
	v_lshl_add_u64 v[12:13], v[12:13], 0, v[170:171]
	v_readlane_b32 s61, v236, 36
	s_and_b64 vcc, exec, s[4:5]
	v_readlane_b32 s62, v236, 37
	v_readlane_b32 s63, v236, 38
	v_readlane_b32 s64, v236, 39
	v_readlane_b32 s65, v236, 40
	v_readlane_b32 s66, v236, 41
	v_readlane_b32 s67, v236, 42
	v_readlane_b32 s68, v236, 43
	v_readlane_b32 s69, v236, 44
	v_readlane_b32 s70, v236, 45
	v_readlane_b32 s71, v236, 46
	v_readlane_b32 s72, v236, 47
	v_readlane_b32 s73, v236, 48
	v_readlane_b32 s74, v236, 49
	v_readlane_b32 s75, v236, 50
	v_pk_fma_f32 v[18:19], v[40:41], s[20:21], v[192:193] op_sel_hi:[1,0,1]
	v_pk_fma_f32 v[20:21], v[38:39], s[20:21], v[190:191] op_sel_hi:[1,0,1]
	v_pk_fma_f32 v[14:15], v[36:37], s[20:21], v[196:197] op_sel_hi:[1,0,1]
	v_pk_fma_f32 v[16:17], v[34:35], s[20:21], v[194:195] op_sel_hi:[1,0,1]
	s_cbranch_vccnz .LBB0_1596
	v_readlane_b32 s60, v236, 24
	v_readlane_b32 s61, v236, 25
	v_cvt_pk_bf16_f32 v22, v20, v21
	v_cvt_pk_bf16_f32 v23, v18, v19
	v_cvt_pk_bf16_f32 v24, v16, v17
	v_cvt_pk_bf16_f32 v25, v14, v15
	v_readlane_b32 s62, v236, 26
	s_nop 0
	v_lshl_add_u64 v[12:13], v[12:13], 1, s[60:61]
	v_readlane_b32 s63, v236, 27
	v_readlane_b32 s64, v236, 28
	v_readlane_b32 s65, v236, 29
	v_readlane_b32 s66, v236, 30
	v_readlane_b32 s67, v236, 31
	global_store_dwordx4 v[12:13], v[22:25], off offset:256

.LBB0_2599:
	v_readlane_b32 s60, v238, 13
	s_ashr_i32 s19, s18, 31
	v_readlane_b32 s62, v238, 15
	v_readlane_b32 s63, v238, 16
	v_readlane_b32 s74, v238, 27
	v_readlane_b32 s75, v238, 28
	s_lshl_b64 s[22:23], s[18:19], 19
	s_mov_b64 s[62:63], s[74:75]
	s_add_u32 s22, s62, s22
	v_readlane_b32 s61, v238, 14
	v_readlane_b32 s64, v238, 17
	v_readlane_b32 s65, v238, 18
	v_readlane_b32 s66, v238, 19
	v_readlane_b32 s67, v238, 20
	v_readlane_b32 s68, v238, 21
	v_readlane_b32 s69, v238, 22
	v_readlane_b32 s70, v238, 23
	v_readlane_b32 s71, v238, 24
	v_readlane_b32 s72, v238, 25
	v_readlane_b32 s73, v238, 26
	s_addc_u32 s23, s63, s23
	s_and_b64 s[24:25], s[0:1], exec
	v_readlane_b32 s60, v237, 45
	s_cselect_b32 s5, s23, s7
	s_cselect_b32 s19, s22, s6
	s_ashr_i32 s21, s20, 31
	s_ashr_i32 s17, s16, 31
	v_readlane_b32 s68, v237, 53
	v_readlane_b32 s69, v237, 54
	s_lshl_b64 s[24:25], s[16:17], 19
	s_lshl_b64 s[36:37], s[20:21], 22
	s_mov_b64 s[48:49], s[68:69]
	s_add_u32 s17, s48, s36
	s_addc_u32 s21, s49, s37
	s_add_u32 s24, s17, s24
	s_addc_u32 s25, s21, s25
	s_and_b64 s[36:37], s[0:1], exec
	s_cselect_b32 s17, s25, s35
	s_cselect_b32 s21, s24, s34
	s_add_u32 s6, s6, 0x40080
	s_addc_u32 s7, s7, 0
	s_add_u32 s31, s34, 0x100
	s_addc_u32 s48, s35, 0
	v_readlane_b32 s98, v237, 35
	v_readlane_b32 s99, v237, 36
	v_lshl_or_b32 v239, s28, 8, v188
	v_lshlrev_b32_e32 v239, 2, v239
	v_lshl_add_u32 v239, s30, 13, v239
	s_nop 4
	global_load_dwordx4 v[240:243], v239, s[98:99]
	global_load_dwordx4 v[244:247], v239, s[98:99] offset:16
	global_load_dwordx4 v[248:251], v239, s[98:99] offset:512
	global_load_dwordx4 v[252:255], v239, s[98:99] offset:528
	s_mov_b32 s49, -2
	v_readlane_b32 s61, v237, 46
	v_readlane_b32 s62, v237, 47
	v_readlane_b32 s63, v237, 48
	v_readlane_b32 s64, v237, 49
	v_readlane_b32 s65, v237, 50
	v_readlane_b32 s66, v237, 51
	v_readlane_b32 s67, v237, 52
	v_readlane_b32 s70, v237, 55
	v_readlane_b32 s71, v237, 56
	v_readlane_b32 s72, v237, 57
	v_readlane_b32 s73, v237, 58
	v_readlane_b32 s74, v237, 59
	v_readlane_b32 s75, v237, 60

.LBB0_2603:
	v_readlane_b32 s60, v237, 29
	s_ashr_i32 s31, s30, 31
	v_readlane_b32 s66, v237, 35
	v_readlane_b32 s67, v237, 36
	s_lshl_b64 s[6:7], s[30:31], 13
	s_mov_b64 s[50:51], s[66:67]
	v_lshl_or_b32 v12, s28, 8, v188
	s_add_u32 s6, s50, s6
	s_addc_u32 s7, s51, s7
	v_ashrrev_i32_e32 v13, 31, v12
	s_nop 15
	s_nop 15
	s_nop 15
	s_lshl_b32 s5, s26, 8
	v_add_u32_e32 v14, s5, v186
	v_add_u32_e32 v16, s5, v187
	v_lshlrev_b64 v[20:21], 1, v[12:13]
	v_add_u32_e32 v24, s5, v1
	v_add_u32_e32 v12, s5, v185
	v_ashrrev_i32_e32 v15, 31, v14
	v_ashrrev_i32_e32 v17, 31, v16
	v_ashrrev_i32_e32 v25, 31, v24
	v_ashrrev_i32_e32 v13, 31, v12
	v_add_u32_e32 v18, 0x80, v24
	v_lshlrev_b64 v[14:15], 12, v[14:15]
	v_lshlrev_b64 v[16:17], 12, v[16:17]
	v_lshlrev_b64 v[22:23], 12, v[24:25]
	v_lshlrev_b64 v[12:13], 12, v[12:13]
	v_ashrrev_i32_e32 v19, 31, v18
	v_lshl_add_u64 v[14:15], s[76:77], 0, v[14:15]
	v_lshl_add_u64 v[26:27], s[76:77], 0, v[16:17]
	v_lshl_add_u64 v[22:23], s[76:77], 0, v[22:23]
	v_lshl_add_u64 v[12:13], s[76:77], 0, v[12:13]
	v_lshlrev_b64 v[28:29], 12, v[18:19]
	v_lshl_add_u64 v[16:17], v[14:15], 0, v[20:21]
	v_lshl_add_u64 v[14:15], v[26:27], 0, v[20:21]
	v_lshl_add_u64 v[22:23], v[22:23], 0, v[20:21]
	v_lshl_add_u64 v[18:19], v[12:13], 0, v[20:21]
	v_lshl_add_u64 v[12:13], s[76:77], 0, v[28:29]
	v_add_u32_e32 v32, 0x90, v24
	v_ashrrev_i32_e32 v33, 31, v32
	v_lshl_add_u64 v[12:13], v[12:13], 0, v[20:21]
	s_andn2_b64 vcc, exec, s[0:1]
	s_mov_b64 s[0:1], -1
	v_readlane_b32 s61, v237, 30
	v_readlane_b32 s62, v237, 31
	v_readlane_b32 s63, v237, 32
	v_readlane_b32 s64, v237, 33
	v_readlane_b32 s65, v237, 34
	v_readlane_b32 s68, v237, 37
	v_readlane_b32 s69, v237, 38
	v_readlane_b32 s70, v237, 39
	v_readlane_b32 s71, v237, 40
	v_readlane_b32 s72, v237, 41
	v_readlane_b32 s73, v237, 42
	v_readlane_b32 s74, v237, 43
	v_readlane_b32 s75, v237, 44
	v_pk_fma_f32 v[26:27], v[98:99], s[14:15], v[240:241] op_sel_hi:[1,0,1]
	v_pk_fma_f32 v[28:29], v[100:101], s[14:15], v[242:243] op_sel_hi:[1,0,1]
	v_cvt_pk_bf16_f32 v26, v26, v27
	v_pk_fma_f32 v[30:31], v[104:105], s[14:15], v[246:247] op_sel_hi:[1,0,1]
	v_cvt_pk_bf16_f32 v27, v28, v29
	v_pk_fma_f32 v[98:99], v[102:103], s[14:15], v[244:245] op_sel_hi:[1,0,1]
	v_pk_fma_f32 v[100:101], v[108:109], s[14:15], v[242:243] op_sel_hi:[1,0,1]
	v_pk_fma_f32 v[102:103], v[106:107], s[14:15], v[240:241] op_sel_hi:[1,0,1]
	v_cvt_pk_bf16_f32 v28, v98, v99
	v_cvt_pk_bf16_f32 v29, v30, v31
	global_store_dwordx4 v[22:23], v[26:29], off
	v_pk_fma_f32 v[104:105], v[112:113], s[14:15], v[246:247] op_sel_hi:[1,0,1]
	v_pk_fma_f32 v[106:107], v[110:111], s[14:15], v[244:245] op_sel_hi:[1,0,1]
	v_cvt_pk_bf16_f32 v26, v102, v103
	v_cvt_pk_bf16_f32 v27, v100, v101
	v_pk_fma_f32 v[108:109], v[116:117], s[14:15], v[242:243] op_sel_hi:[1,0,1]
	v_pk_fma_f32 v[110:111], v[114:115], s[14:15], v[240:241] op_sel_hi:[1,0,1]
	v_cvt_pk_bf16_f32 v28, v106, v107
	v_cvt_pk_bf16_f32 v29, v104, v105
	global_store_dwordx4 v[18:19], v[26:29], off
	v_pk_fma_f32 v[112:113], v[120:121], s[14:15], v[246:247] op_sel_hi:[1,0,1]
	v_pk_fma_f32 v[114:115], v[118:119], s[14:15], v[244:245] op_sel_hi:[1,0,1]
	v_cvt_pk_bf16_f32 v26, v110, v111
	v_cvt_pk_bf16_f32 v27, v108, v109
	v_pk_fma_f32 v[116:117], v[132:133], s[14:15], v[242:243] op_sel_hi:[1,0,1]
	v_pk_fma_f32 v[118:119], v[130:131], s[14:15], v[240:241] op_sel_hi:[1,0,1]
	v_cvt_pk_bf16_f32 v28, v114, v115
	v_cvt_pk_bf16_f32 v29, v112, v113
	global_store_dwordx4 v[16:17], v[26:29], off
	v_pk_fma_f32 v[120:121], v[136:137], s[14:15], v[246:247] op_sel_hi:[1,0,1]
	v_pk_fma_f32 v[130:131], v[134:135], s[14:15], v[244:245] op_sel_hi:[1,0,1]
	v_cvt_pk_bf16_f32 v26, v118, v119
	v_cvt_pk_bf16_f32 v27, v116, v117
	v_pk_fma_f32 v[132:133], v[148:149], s[14:15], v[242:243] op_sel_hi:[1,0,1]
	v_pk_fma_f32 v[134:135], v[146:147], s[14:15], v[240:241] op_sel_hi:[1,0,1]
	v_cvt_pk_bf16_f32 v28, v130, v131
	v_cvt_pk_bf16_f32 v29, v120, v121
	global_store_dwordx4 v[14:15], v[26:29], off
	v_pk_fma_f32 v[136:137], v[152:153], s[14:15], v[246:247] op_sel_hi:[1,0,1]
	v_pk_fma_f32 v[146:147], v[150:151], s[14:15], v[244:245] op_sel_hi:[1,0,1]
	v_cvt_pk_bf16_f32 v26, v134, v135
	v_cvt_pk_bf16_f32 v27, v132, v133
	v_pk_fma_f32 v[148:149], v[156:157], s[14:15], v[242:243] op_sel_hi:[1,0,1]
	v_cvt_pk_bf16_f32 v28, v146, v147
	v_cvt_pk_bf16_f32 v29, v136, v137
	global_store_dwordx4 v[12:13], v[26:29], off
	v_pk_fma_f32 v[150:151], v[154:155], s[14:15], v[240:241] op_sel_hi:[1,0,1]
	v_pk_fma_f32 v[152:153], v[160:161], s[14:15], v[246:247] op_sel_hi:[1,0,1]
	v_lshlrev_b64 v[26:27], 12, v[32:33]
	v_lshl_add_u64 v[26:27], s[76:77], 0, v[26:27]
	v_pk_fma_f32 v[154:155], v[158:159], s[14:15], v[244:245] op_sel_hi:[1,0,1]
	v_cvt_pk_bf16_f32 v28, v150, v151
	v_cvt_pk_bf16_f32 v29, v148, v149
	v_lshl_add_u64 v[26:27], v[26:27], 0, v[20:21]
	v_cvt_pk_bf16_f32 v30, v154, v155
	v_cvt_pk_bf16_f32 v31, v152, v153
	global_store_dwordx4 v[26:27], v[28:31], off
	v_pk_fma_f32 v[32:33], v[144:145], s[14:15], v[246:247] op_sel_hi:[1,0,1]
	v_pk_fma_f32 v[98:99], v[142:143], s[14:15], v[244:245] op_sel_hi:[1,0,1]
	v_pk_fma_f32 v[30:31], v[140:141], s[14:15], v[242:243] op_sel_hi:[1,0,1]
	v_pk_fma_f32 v[28:29], v[138:139], s[14:15], v[240:241] op_sel_hi:[1,0,1]
	v_pk_fma_f32 v[6:7], v[122:123], s[14:15], v[240:241] op_sel_hi:[1,0,1]
	v_cvt_pk_bf16_f32 v28, v28, v29
	v_cvt_pk_bf16_f32 v29, v30, v31
	v_cvt_pk_bf16_f32 v30, v98, v99
	v_cvt_pk_bf16_f32 v31, v32, v33
	v_add_u32_e32 v32, 0xa0, v24
	v_ashrrev_i32_e32 v33, 31, v32
	v_lshlrev_b64 v[32:33], 12, v[32:33]
	v_lshl_add_u64 v[32:33], s[76:77], 0, v[32:33]
	v_lshl_add_u64 v[32:33], v[32:33], 0, v[20:21]
	global_store_dwordx4 v[32:33], v[28:31], off
	v_pk_fma_f32 v[8:9], v[124:125], s[14:15], v[242:243] op_sel_hi:[1,0,1]
	s_nop 0
	v_pk_fma_f32 v[28:29], v[128:129], s[14:15], v[246:247] op_sel_hi:[1,0,1]
	v_pk_fma_f32 v[4:5], v[126:127], s[14:15], v[244:245] op_sel_hi:[1,0,1]
	v_cvt_pk_bf16_f32 v2, v6, v7
	v_add_u32_e32 v6, 0xb0, v24
	v_ashrrev_i32_e32 v7, 31, v6
	v_lshlrev_b64 v[6:7], 12, v[6:7]
	v_lshl_add_u64 v[6:7], s[76:77], 0, v[6:7]
	v_lshl_add_u64 v[24:25], v[6:7], 0, v[20:21]
	v_cvt_pk_bf16_f32 v3, v8, v9
	v_cvt_pk_bf16_f32 v4, v4, v5
	v_cvt_pk_bf16_f32 v5, v28, v29
	global_store_dwordx4 v[24:25], v[2:5], off
	s_nop 0
	v_pk_fma_f32 v[20:21], v[94:95], s[14:15], v[248:249] op_sel_hi:[1,0,1]
	v_pk_fma_f32 v[30:31], v[90:91], s[14:15], v[252:253] op_sel_hi:[1,0,1]
	v_pk_fma_f32 v[10:11], v[96:97], s[14:15], v[250:251] op_sel_hi:[1,0,1]
	v_pk_fma_f32 v[92:93], v[92:93], s[14:15], v[254:255] op_sel_hi:[1,0,1]
	v_pk_fma_f32 v[84:85], v[84:85], s[14:15], v[250:251] op_sel_hi:[1,0,1]
	v_pk_fma_f32 v[82:83], v[82:83], s[14:15], v[248:249] op_sel_hi:[1,0,1]
	v_cvt_pk_bf16_f32 v28, v20, v21
	v_cvt_pk_bf16_f32 v29, v10, v11
	v_cvt_pk_bf16_f32 v30, v30, v31
	v_cvt_pk_bf16_f32 v31, v92, v93
	global_store_dwordx4 v[22:23], v[28:31], off offset:256
	v_cvt_pk_bf16_f32 v20, v82, v83
	v_cvt_pk_bf16_f32 v21, v84, v85
	v_pk_fma_f32 v[88:89], v[88:89], s[14:15], v[254:255] op_sel_hi:[1,0,1]
	v_pk_fma_f32 v[86:87], v[86:87], s[14:15], v[252:253] op_sel_hi:[1,0,1]
	v_pk_fma_f32 v[68:69], v[68:69], s[14:15], v[250:251] op_sel_hi:[1,0,1]
	v_pk_fma_f32 v[66:67], v[66:67], s[14:15], v[248:249] op_sel_hi:[1,0,1]
	v_pk_fma_f32 v[72:73], v[72:73], s[14:15], v[254:255] op_sel_hi:[1,0,1]
	v_pk_fma_f32 v[70:71], v[70:71], s[14:15], v[252:253] op_sel_hi:[1,0,1]
	v_pk_fma_f32 v[52:53], v[52:53], s[14:15], v[250:251] op_sel_hi:[1,0,1]
	v_pk_fma_f32 v[50:51], v[50:51], s[14:15], v[248:249] op_sel_hi:[1,0,1]
	v_cvt_pk_bf16_f32 v22, v86, v87
	v_cvt_pk_bf16_f32 v23, v88, v89
	global_store_dwordx4 v[18:19], v[20:23], off offset:256
	v_cvt_pk_bf16_f32 v18, v66, v67
	v_cvt_pk_bf16_f32 v19, v68, v69
	v_pk_fma_f32 v[56:57], v[56:57], s[14:15], v[254:255] op_sel_hi:[1,0,1]
	v_pk_fma_f32 v[54:55], v[54:55], s[14:15], v[252:253] op_sel_hi:[1,0,1]
	v_cvt_pk_bf16_f32 v20, v70, v71
	v_cvt_pk_bf16_f32 v21, v72, v73
	global_store_dwordx4 v[16:17], v[18:21], off offset:256
	v_cvt_pk_bf16_f32 v16, v50, v51
	v_cvt_pk_bf16_f32 v17, v52, v53
	v_pk_fma_f32 v[76:77], v[76:77], s[14:15], v[250:251] op_sel_hi:[1,0,1]
	v_pk_fma_f32 v[74:75], v[74:75], s[14:15], v[248:249] op_sel_hi:[1,0,1]
	v_pk_fma_f32 v[80:81], v[80:81], s[14:15], v[254:255] op_sel_hi:[1,0,1]
	v_pk_fma_f32 v[78:79], v[78:79], s[14:15], v[252:253] op_sel_hi:[1,0,1]
	v_pk_fma_f32 v[60:61], v[60:61], s[14:15], v[250:251] op_sel_hi:[1,0,1]
	v_pk_fma_f32 v[58:59], v[58:59], s[14:15], v[248:249] op_sel_hi:[1,0,1]
	v_pk_fma_f32 v[64:65], v[64:65], s[14:15], v[254:255] op_sel_hi:[1,0,1]
	v_pk_fma_f32 v[62:63], v[62:63], s[14:15], v[252:253] op_sel_hi:[1,0,1]
	v_cvt_pk_bf16_f32 v18, v54, v55
	v_cvt_pk_bf16_f32 v19, v56, v57
	global_store_dwordx4 v[14:15], v[16:19], off offset:256
	v_cvt_pk_bf16_f32 v14, v74, v75
	v_cvt_pk_bf16_f32 v15, v76, v77
	v_pk_fma_f32 v[48:49], v[48:49], s[14:15], v[250:251] op_sel_hi:[1,0,1]
	v_pk_fma_f32 v[46:47], v[46:47], s[14:15], v[248:249] op_sel_hi:[1,0,1]
	v_cvt_pk_bf16_f32 v16, v78, v79
	v_cvt_pk_bf16_f32 v17, v80, v81
	global_store_dwordx4 v[12:13], v[14:17], off offset:256
	v_cvt_pk_bf16_f32 v10, v58, v59
	v_cvt_pk_bf16_f32 v11, v60, v61
	v_cvt_pk_bf16_f32 v12, v62, v63
	v_cvt_pk_bf16_f32 v13, v64, v65
	v_pk_fma_f32 v[44:45], v[44:45], s[14:15], v[254:255] op_sel_hi:[1,0,1]
	global_store_dwordx4 v[26:27], v[10:13], off offset:256
	v_pk_fma_f32 v[4:5], v[40:41], s[14:15], v[250:251] op_sel_hi:[1,0,1]
	v_pk_fma_f32 v[2:3], v[38:39], s[14:15], v[248:249] op_sel_hi:[1,0,1]
	v_pk_fma_f32 v[12:13], v[42:43], s[14:15], v[252:253] op_sel_hi:[1,0,1]
	v_cvt_pk_bf16_f32 v10, v46, v47
	v_cvt_pk_bf16_f32 v11, v48, v49
	v_pk_fma_f32 v[8:9], v[36:37], s[14:15], v[254:255] op_sel_hi:[1,0,1]
	v_cvt_pk_bf16_f32 v12, v12, v13
	v_cvt_pk_bf16_f32 v13, v44, v45
	global_store_dwordx4 v[32:33], v[10:13], off offset:256
	v_pk_fma_f32 v[6:7], v[34:35], s[14:15], v[252:253] op_sel_hi:[1,0,1]
	v_cvt_pk_bf16_f32 v2, v2, v3
	v_cvt_pk_bf16_f32 v3, v4, v5
	s_nop 0
	v_cvt_pk_bf16_f32 v4, v6, v7
	v_cvt_pk_bf16_f32 v5, v8, v9
	global_store_dwordx4 v[24:25], v[2:5], off offset:256
	s_cbranch_vccnz .LBB0_2596
	s_mov_b32 s6, s4
	s_mov_b32 s7, s4
	s_mov_b32 s5, s4
	v_mov_b64_e32 v[36:37], s[6:7]
	v_mov_b64_e32 v[100:101], s[6:7]
	v_mov_b64_e32 v[104:105], s[6:7]
	v_mov_b64_e32 v[108:109], s[6:7]
	v_mov_b64_e32 v[112:113], s[6:7]
	v_mov_b64_e32 v[116:117], s[6:7]
	v_mov_b64_e32 v[120:121], s[6:7]
	v_mov_b64_e32 v[132:133], s[6:7]
	v_mov_b64_e32 v[136:137], s[6:7]
	v_mov_b64_e32 v[96:97], s[6:7]
	v_mov_b64_e32 v[92:93], s[6:7]
	v_mov_b64_e32 v[84:85], s[6:7]
	v_mov_b64_e32 v[88:89], s[6:7]
	v_mov_b64_e32 v[68:69], s[6:7]
	v_mov_b64_e32 v[72:73], s[6:7]
	v_mov_b64_e32 v[52:53], s[6:7]
	v_mov_b64_e32 v[56:57], s[6:7]
	v_mov_b64_e32 v[148:149], s[6:7]
	v_mov_b64_e32 v[152:153], s[6:7]
	v_mov_b64_e32 v[156:157], s[6:7]
	v_mov_b64_e32 v[160:161], s[6:7]
	v_mov_b64_e32 v[140:141], s[6:7]
	v_mov_b64_e32 v[144:145], s[6:7]
	v_mov_b64_e32 v[124:125], s[6:7]
	v_mov_b64_e32 v[128:129], s[6:7]
	v_mov_b64_e32 v[76:77], s[6:7]
	v_mov_b64_e32 v[80:81], s[6:7]
	v_mov_b64_e32 v[60:61], s[6:7]
	v_mov_b64_e32 v[64:65], s[6:7]
	v_mov_b64_e32 v[48:49], s[6:7]
	v_mov_b64_e32 v[44:45], s[6:7]
	v_mov_b64_e32 v[40:41], s[6:7]
	v_mov_b64_e32 v[34:35], s[4:5]
	v_mov_b64_e32 v[98:99], s[4:5]
	v_mov_b64_e32 v[102:103], s[4:5]
	v_mov_b64_e32 v[106:107], s[4:5]
	v_mov_b64_e32 v[110:111], s[4:5]
	v_mov_b64_e32 v[114:115], s[4:5]
	v_mov_b64_e32 v[118:119], s[4:5]
	v_mov_b64_e32 v[130:131], s[4:5]
	v_mov_b64_e32 v[134:135], s[4:5]
	v_mov_b64_e32 v[94:95], s[4:5]
	v_mov_b64_e32 v[90:91], s[4:5]
	v_mov_b64_e32 v[82:83], s[4:5]
	v_mov_b64_e32 v[86:87], s[4:5]
	v_mov_b64_e32 v[66:67], s[4:5]
	v_mov_b64_e32 v[70:71], s[4:5]
	v_mov_b64_e32 v[50:51], s[4:5]
	v_mov_b64_e32 v[54:55], s[4:5]
	v_mov_b64_e32 v[146:147], s[4:5]
	v_mov_b64_e32 v[150:151], s[4:5]
	v_mov_b64_e32 v[154:155], s[4:5]
	v_mov_b64_e32 v[158:159], s[4:5]
	v_mov_b64_e32 v[138:139], s[4:5]
	v_mov_b64_e32 v[142:143], s[4:5]
	v_mov_b64_e32 v[122:123], s[4:5]
	v_mov_b64_e32 v[126:127], s[4:5]
	v_mov_b64_e32 v[74:75], s[4:5]
	v_mov_b64_e32 v[78:79], s[4:5]
	v_mov_b64_e32 v[58:59], s[4:5]
	v_mov_b64_e32 v[62:63], s[4:5]
	v_mov_b64_e32 v[46:47], s[4:5]
	v_mov_b64_e32 v[42:43], s[4:5]
	v_mov_b64_e32 v[38:39], s[4:5]
	s_andn2_b64 vcc, exec, s[8:9]
	s_cbranch_vccnz .LBB0_2595
	s_barrier
	s_branch .LBB0_2595
